# P5 and P6: within every XCD the workgroups with blockIdx bit 4 set start ~13us late (epilogue bursts of the two sub-groups no longer coincide)
# speedup vs baseline: 1.0077x; 1.0074x over previous
; #define REP(k) for (int rep_ = reframe(F); rep_ < (((MK_DUP) >> (k)) & 1) + 1; ++rep_)
; __global__ void __launch_bounds__(NTHREADS, 2) mk_fwd(Args args) {
;     ...
;     if (IN(5)) REP(5) {
;         { pg8::DenseSched S; S.init((const bf16_t*)(F.ws + WS_SG), GW, (const bf16_t*)(F.ws + WS_WPA), GW, T, D, F.G, (int)blockIdx.x); EpiMerge<0> E{F.ws}; pg8::gemm_phase<0>(F.lds, S, E); }
.LBB0_559:
	s_cmp_lt_i32 s88, 6
	s_cselect_b64 s[4:5], -1, 0
	s_and_b64 s[4:5], s[4:5], s[0:1]
	s_andn2_b64 vcc, exec, s[4:5]
	s_cbranch_vccnz .LBB0_620
	s_and_b32 s98, s92, 16
	s_cmp_eq_u32 s98, 0
	s_cbranch_scc1 .Lstag5_done
	s_sleep 127
	s_sleep 127
	s_sleep 127

; #define REP(k) for (int rep_ = reframe(F); rep_ < (((MK_DUP) >> (k)) & 1) + 1; ++rep_)
; #define REPBAR(k) do { if ((((MK_DUP) >> (k)) & 1) && rep_ == 0) xcd_barrier(bar); } while (0)
; __global__ void __launch_bounds__(NTHREADS, 2) mk_fwd(Args args) {
;     ...
;     if (IN(6)) REP(6) {
;         pg8::DenseSched S; S.init((const bf16_t*)(F.ws + WS_MRG), D, (const bf16_t*)(F.ws + WS_WOUT), D, T, D, F.G, (int)blockIdx.x);
;         EpiOut E{args.in[0], F.ws};
;         pg8::gemm_phase<0>(F.lds, S, E); REPBAR(6);
.LBB0_674:
	s_cmp_lt_i32 s88, 7
	s_cselect_b64 s[4:5], -1, 0
	s_and_b64 s[4:5], s[4:5], s[0:1]
	s_andn2_b64 vcc, exec, s[4:5]
	s_cbranch_vccnz .LBB0_723
	s_and_b32 s98, s92, 16
	s_cmp_eq_u32 s98, 0
	s_cbranch_scc1 .Lstag6_done
	s_sleep 127
	s_sleep 127
	s_sleep 127
